# attention hot loop: first step's 8 PV MFMAs moved back before the step barrier, interleaved with its exp groups (balances MFMAs 16/16 between the two barrier intervals)
# speedup vs baseline: 1.0350x; 1.0003x over previous
.LBB0_1702:
	s_mov_b32 s8, s53
	s_mov_b32 s41, s52
	ds_read_b128 v[36:39], v35
	ds_read_b128 v[40:43], v35 offset:32
	ds_read_b128 v[44:47], v35 offset:64
	ds_read_b128 v[82:85], v35 offset:96
	ds_read_b128 v[178:181], v35 offset:128
	ds_read_b128 v[86:89], v35 offset:160
	ds_read_b128 v[90:93], v35 offset:192
	ds_read_b128 v[94:97], v35 offset:224
	s_waitcnt lgkmcnt(4)
	v_sub_f32_e32 v113, v213, v85
	v_sub_f32_e32 v112, v213, v84
	v_sub_f32_e32 v111, v213, v83
	v_sub_f32_e32 v110, v213, v82
	v_sub_f32_e32 v109, v213, v47
	v_sub_f32_e32 v108, v213, v46
	v_sub_f32_e32 v107, v213, v45
	v_sub_f32_e32 v106, v213, v44
	v_sub_f32_e32 v105, v213, v43
	v_sub_f32_e32 v104, v213, v42
	v_sub_f32_e32 v103, v213, v41
	v_sub_f32_e32 v102, v213, v40
	v_sub_f32_e32 v101, v213, v39
	v_sub_f32_e32 v100, v213, v38
	v_sub_f32_e32 v99, v213, v37
	v_sub_f32_e32 v98, v213, v36
	s_waitcnt lgkmcnt(0)
	v_sub_f32_e32 v97, v213, v97
	v_sub_f32_e32 v96, v213, v96
	v_sub_f32_e32 v95, v213, v95
	v_sub_f32_e32 v94, v213, v94
	v_sub_f32_e32 v93, v213, v93
	v_sub_f32_e32 v92, v213, v92
	v_sub_f32_e32 v91, v213, v91
	v_sub_f32_e32 v90, v213, v90
	v_sub_f32_e32 v89, v213, v89
	v_sub_f32_e32 v88, v213, v88
	v_sub_f32_e32 v87, v213, v87
	v_sub_f32_e32 v86, v213, v86
	v_sub_f32_e32 v85, v213, v181
	v_sub_f32_e32 v84, v213, v180
	v_sub_f32_e32 v83, v213, v179
	v_sub_f32_e32 v82, v213, v178
	v_add_u32_e32 v178, s42, v235
	ds_read_b64_tr_b16 v[36:37], v178 offset:24576
	ds_read_b64_tr_b16 v[38:39], v178 offset:25088
	v_add_f32_e32 v40, v66, v67
	v_add_f32_e32 v40, v68, v40
	v_add_f32_e32 v40, v69, v40
	v_add_f32_e32 v40, v70, v40
	v_add_f32_e32 v44, v71, v40
	v_cvt_pk_bf16_f32 v130, v66, v67
	v_cvt_pk_bf16_f32 v131, v68, v69
	v_mfma_f32_32x32x16_bf16 v[98:113], v[174:177], v[114:117], v[98:113]
	ds_read_b64_tr_b16 v[40:41], v178 offset:28672
	ds_read_b64_tr_b16 v[42:43], v178 offset:29184
	v_add_f32_e32 v44, v72, v44
	v_add_f32_e32 v44, v73, v44
	v_add_f32_e32 v44, v74, v44
	v_add_f32_e32 v48, v75, v44
	v_cvt_pk_bf16_f32 v132, v70, v71
	v_cvt_pk_bf16_f32 v133, v72, v73
	v_mfma_f32_32x32x16_bf16 v[82:97], v[166:169], v[114:117], v[82:97]
	ds_read_b64_tr_b16 v[44:45], v178 offset:25600
	ds_read_b64_tr_b16 v[46:47], v178 offset:26112
	v_add_f32_e32 v48, v76, v48
	v_add_f32_e32 v48, v77, v48
	v_add_f32_e32 v48, v78, v48
	v_add_f32_e32 v48, v79, v48
	v_cvt_pk_bf16_f32 v134, v74, v75
	v_cvt_pk_bf16_f32 v135, v76, v77
	v_mfma_f32_32x32x16_bf16 v[98:113], v[170:173], v[118:121], v[98:113]
	ds_read_b64_tr_b16 v[66:67], v178 offset:29696
	ds_read_b64_tr_b16 v[68:69], v178 offset:30208
	v_add_f32_e32 v48, v80, v48
	v_add_f32_e32 v48, v81, v48
	v_add_f32_e32 v48, v50, v48
	v_add_f32_e32 v48, v51, v48
	v_cvt_pk_bf16_f32 v136, v78, v79
	v_cvt_pk_bf16_f32 v137, v80, v81
	v_mfma_f32_32x32x16_bf16 v[82:97], v[158:161], v[118:121], v[82:97]
	ds_read_b64_tr_b16 v[158:159], v178 offset:26624
	ds_read_b64_tr_b16 v[160:161], v178 offset:27136
	v_add_f32_e32 v48, v52, v48
	v_add_f32_e32 v48, v53, v48
	v_add_f32_e32 v48, v54, v48
	v_add_f32_e32 v70, v55, v48
	v_cvt_pk_bf16_f32 v138, v50, v51
	v_cvt_pk_bf16_f32 v139, v52, v53
	v_mfma_f32_32x32x16_bf16 v[98:113], v[162:165], v[122:125], v[98:113]
	ds_read_b64_tr_b16 v[48:49], v178 offset:30720
	ds_read_b64_tr_b16 v[50:51], v178 offset:31232
	v_add_f32_e32 v52, v56, v70
	v_add_f32_e32 v52, v57, v52
	v_add_f32_e32 v52, v58, v52
	v_add_f32_e32 v52, v59, v52
	v_cvt_pk_bf16_f32 v140, v54, v55
	v_cvt_pk_bf16_f32 v141, v56, v57
	v_mfma_f32_32x32x16_bf16 v[82:97], v[150:153], v[122:125], v[82:97]
	ds_read_b64_tr_b16 v[150:151], v178 offset:27648
	ds_read_b64_tr_b16 v[152:153], v178 offset:28160
	v_add_f32_e32 v52, v60, v52
	v_add_f32_e32 v52, v61, v52
	v_add_f32_e32 v52, v62, v52
	v_add_f32_e32 v52, v63, v52
	v_cvt_pk_bf16_f32 v142, v58, v59
	v_cvt_pk_bf16_f32 v143, v60, v61
	v_mfma_f32_32x32x16_bf16 v[98:113], v[154:157], v[126:129], v[98:113]
	ds_read_b64_tr_b16 v[166:167], v178 offset:31744
	ds_read_b64_tr_b16 v[168:169], v178 offset:32256
	v_add_f32_e32 v52, v64, v52
	v_add_f32_e32 v52, v65, v52
	v_add_f32_e32 v251, 0, v52
	v_cvt_pk_bf16_f32 v144, v62, v63
	v_cvt_pk_bf16_f32 v145, v64, v65
	v_mfma_f32_32x32x16_bf16 v[82:97], v[146:149], v[126:129], v[82:97]
	v_lshl_add_u64 v[52:53], v[220:221], 0, s[20:21]
	s_add_i32 s42, s52, s50
	s_mov_b32 s43, m0
	s_mov_b32 m0, s42
	s_nop 0
	global_load_lds_dwordx4 v[52:53], off
	s_mov_b32 m0, s43
	v_lshl_add_u64 v[52:53], v[218:219], 0, s[20:21]
	s_add_i32 s42, s53, s51
	s_mov_b32 s43, m0
	s_mov_b32 m0, s42
	s_nop 0
	global_load_lds_dwordx4 v[52:53], off
	s_mov_b32 m0, s43
	s_waitcnt lgkmcnt(14)
	v_mfma_f32_32x32x16_bf16 v[2:17], v[130:133], v[36:39], v[2:17]
	v_exp_f32_e32 v98, v98
	v_exp_f32_e32 v99, v99
	v_exp_f32_e32 v100, v100
	v_exp_f32_e32 v101, v101
	s_nop 0
	s_waitcnt lgkmcnt(12)
	v_mfma_f32_32x32x16_bf16 v[18:33], v[130:133], v[40:43], v[18:33]
	v_exp_f32_e32 v102, v102
	v_exp_f32_e32 v103, v103
	v_exp_f32_e32 v104, v104
	v_exp_f32_e32 v105, v105
	v_add_u32_e32 v52, s8, v232
	ds_read_b128 v[186:189], v52
	ds_read_b128 v[178:181], v52 offset:512
	s_waitcnt lgkmcnt(12)
	v_mfma_f32_32x32x16_bf16 v[2:17], v[134:137], v[44:47], v[2:17]
	v_exp_f32_e32 v106, v106
	v_exp_f32_e32 v107, v107
	v_exp_f32_e32 v108, v108
	v_exp_f32_e32 v109, v109
	ds_read_b128 v[182:185], v52 offset:2048
	ds_read_b128 v[170:173], v52 offset:2560
	s_waitcnt lgkmcnt(12)
	v_mfma_f32_32x32x16_bf16 v[18:33], v[134:137], v[66:69], v[18:33]
	v_exp_f32_e32 v110, v110
	v_exp_f32_e32 v111, v111
	v_exp_f32_e32 v112, v112
	v_exp_f32_e32 v113, v113
	ds_read_b128 v[174:177], v52 offset:4096
	ds_read_b128 v[154:157], v52 offset:4608
	s_waitcnt lgkmcnt(12)
	v_mfma_f32_32x32x16_bf16 v[2:17], v[138:141], v[158:161], v[2:17]
	v_exp_f32_e32 v82, v82
	v_exp_f32_e32 v83, v83
	v_exp_f32_e32 v84, v84
	v_exp_f32_e32 v85, v85
	ds_read_b128 v[162:165], v52 offset:6144
	ds_read_b128 v[146:149], v52 offset:6656
	s_waitcnt lgkmcnt(12)
	v_mfma_f32_32x32x16_bf16 v[18:33], v[138:141], v[48:51], v[18:33]
	v_exp_f32_e32 v86, v86
	v_exp_f32_e32 v87, v87
	v_exp_f32_e32 v88, v88
	v_exp_f32_e32 v89, v89
	s_nop 0
	s_waitcnt lgkmcnt(10)
	v_mfma_f32_32x32x16_bf16 v[2:17], v[142:145], v[150:153], v[2:17]
	v_exp_f32_e32 v90, v90
	v_exp_f32_e32 v91, v91
	v_exp_f32_e32 v92, v92
	v_exp_f32_e32 v93, v93
	s_nop 0
	s_waitcnt lgkmcnt(8)
	v_mfma_f32_32x32x16_bf16 v[18:33], v[142:145], v[166:169], v[18:33]
	v_exp_f32_e32 v94, v94
	v_exp_f32_e32 v95, v95
	v_exp_f32_e32 v96, v96
	v_exp_f32_e32 v97, v97
	s_waitcnt vmcnt(2) lgkmcnt(0)
	s_barrier
	s_add_i32 s42, s53, 0x2000
	s_cmpk_lg_i32 s53, 0x4000
	v_add_f32_e32 v34, v34, v251
	s_cselect_b32 s52, s42, 0
	ds_read_b128 v[36:39], v35 offset:256
	ds_read_b128 v[40:43], v35 offset:288
	ds_read_b128 v[52:55], v35 offset:320
	ds_read_b128 v[56:59], v35 offset:352
	ds_read_b128 v[242:245], v35 offset:384
	ds_read_b128 v[246:249], v35 offset:416
	ds_read_b128 v[190:193], v35 offset:448
	ds_read_b128 v[60:63], v35 offset:480
	s_waitcnt lgkmcnt(4)
	v_sub_f32_e32 v81, v213, v59
	v_sub_f32_e32 v80, v213, v58
	v_sub_f32_e32 v79, v213, v57
	v_sub_f32_e32 v78, v213, v56
	v_sub_f32_e32 v77, v213, v55
	v_sub_f32_e32 v76, v213, v54
	v_sub_f32_e32 v75, v213, v53
	v_sub_f32_e32 v74, v213, v52
	v_sub_f32_e32 v73, v213, v43
	v_sub_f32_e32 v72, v213, v42
	v_sub_f32_e32 v71, v213, v41
	v_sub_f32_e32 v70, v213, v40
	s_waitcnt lgkmcnt(0)
	v_sub_f32_e32 v65, v213, v63
	v_sub_f32_e32 v69, v213, v39
	v_sub_f32_e32 v68, v213, v38
	v_sub_f32_e32 v67, v213, v37
	v_sub_f32_e32 v66, v213, v36
	v_sub_f32_e32 v64, v213, v62
	v_sub_f32_e32 v63, v213, v61
	v_sub_f32_e32 v62, v213, v60
	v_sub_f32_e32 v61, v213, v193
	v_sub_f32_e32 v60, v213, v192
	v_sub_f32_e32 v59, v213, v191
	v_sub_f32_e32 v58, v213, v190
	v_sub_f32_e32 v57, v213, v249
	v_sub_f32_e32 v56, v213, v248
	v_sub_f32_e32 v55, v213, v247
	v_sub_f32_e32 v54, v213, v246
	v_sub_f32_e32 v53, v213, v245
	v_sub_f32_e32 v52, v213, v244
	v_sub_f32_e32 v51, v213, v243
	v_sub_f32_e32 v50, v213, v242
	v_add_u32_e32 v48, s41, v235
	ds_read_b64_tr_b16 v[36:37], v48 offset:24576
	ds_read_b64_tr_b16 v[38:39], v48 offset:25088
	v_mfma_f32_32x32x16_bf16 v[66:81], v[186:189], v[114:117], v[66:81]
	v_add_f32_e32 v40, v98, v99
	v_add_f32_e32 v40, v100, v40
	v_add_f32_e32 v40, v101, v40
	v_add_f32_e32 v40, v102, v40
	v_add_f32_e32 v44, v103, v40
	v_cvt_pk_bf16_f32 v130, v98, v99
	v_cvt_pk_bf16_f32 v131, v100, v101
	ds_read_b64_tr_b16 v[40:41], v48 offset:28672
	ds_read_b64_tr_b16 v[42:43], v48 offset:29184
	v_mfma_f32_32x32x16_bf16 v[50:65], v[178:181], v[114:117], v[50:65]
	v_add_f32_e32 v44, v104, v44
	v_add_f32_e32 v44, v105, v44
	v_add_f32_e32 v44, v106, v44
	v_add_f32_e32 v49, v107, v44
	v_cvt_pk_bf16_f32 v132, v102, v103
	v_cvt_pk_bf16_f32 v133, v104, v105
	ds_read_b64_tr_b16 v[44:45], v48 offset:25600
	ds_read_b64_tr_b16 v[46:47], v48 offset:26112
	v_mfma_f32_32x32x16_bf16 v[66:81], v[182:185], v[118:121], v[66:81]
	v_add_f32_e32 v49, v108, v49
	v_add_f32_e32 v49, v109, v49
	v_add_f32_e32 v49, v110, v49
	v_add_f32_e32 v49, v111, v49
	v_cvt_pk_bf16_f32 v134, v106, v107
	v_cvt_pk_bf16_f32 v135, v108, v109
	ds_read_b64_tr_b16 v[98:99], v48 offset:29696
	ds_read_b64_tr_b16 v[100:101], v48 offset:30208
	v_mfma_f32_32x32x16_bf16 v[50:65], v[170:173], v[118:121], v[50:65]
	v_add_f32_e32 v49, v112, v49
	v_add_f32_e32 v49, v113, v49
	v_add_f32_e32 v49, v82, v49
	v_add_f32_e32 v49, v83, v49
	v_cvt_pk_bf16_f32 v136, v110, v111
	v_cvt_pk_bf16_f32 v137, v112, v113
	ds_read_b64_tr_b16 v[102:103], v48 offset:26624
	ds_read_b64_tr_b16 v[104:105], v48 offset:27136
	v_mfma_f32_32x32x16_bf16 v[66:81], v[174:177], v[122:125], v[66:81]
	v_add_f32_e32 v49, v84, v49
	v_add_f32_e32 v49, v85, v49
	v_add_f32_e32 v49, v86, v49
	v_add_f32_e32 v49, v87, v49
	v_cvt_pk_bf16_f32 v138, v82, v83
	v_cvt_pk_bf16_f32 v139, v84, v85
	ds_read_b64_tr_b16 v[82:83], v48 offset:30720
	ds_read_b64_tr_b16 v[84:85], v48 offset:31232
	v_mfma_f32_32x32x16_bf16 v[50:65], v[154:157], v[122:125], v[50:65]
	v_add_f32_e32 v49, v88, v49
	v_add_f32_e32 v49, v89, v49
	v_add_f32_e32 v49, v90, v49
	v_add_f32_e32 v49, v91, v49
	v_cvt_pk_bf16_f32 v140, v86, v87
	v_cvt_pk_bf16_f32 v141, v88, v89
	ds_read_b64_tr_b16 v[86:87], v48 offset:27648
	ds_read_b64_tr_b16 v[88:89], v48 offset:28160
	v_mfma_f32_32x32x16_bf16 v[66:81], v[162:165], v[126:129], v[66:81]
	v_add_f32_e32 v49, v92, v49
	v_add_f32_e32 v49, v93, v49
	v_add_f32_e32 v49, v94, v49
	v_add_f32_e32 v49, v95, v49
	v_cvt_pk_bf16_f32 v142, v90, v91
	v_cvt_pk_bf16_f32 v143, v92, v93
	ds_read_b64_tr_b16 v[90:91], v48 offset:31744
	ds_read_b64_tr_b16 v[92:93], v48 offset:32256
	v_mfma_f32_32x32x16_bf16 v[50:65], v[146:149], v[126:129], v[50:65]
	v_add_f32_e32 v48, v96, v49
	v_add_f32_e32 v48, v97, v48
	v_add_f32_e32 v48, 0, v48
	v_cvt_pk_bf16_f32 v144, v94, v95
	v_cvt_pk_bf16_f32 v145, v96, v97
	s_add_i32 s41, s53, s50
	s_mov_b32 s42, m0
	s_mov_b32 m0, s41
	s_nop 0
	global_load_lds_dwordx4 v[220:221], off
	s_mov_b32 m0, s42
	s_add_i32 s41, s52, s51
	s_mov_b32 s42, m0
	s_mov_b32 m0, s41
	s_nop 0
	global_load_lds_dwordx4 v[218:219], off
	s_mov_b32 m0, s42
	v_add_f32_e32 v34, v34, v48
	s_add_i32 s30, s30, 2
	s_waitcnt lgkmcnt(14)
	v_mfma_f32_32x32x16_bf16 v[2:17], v[130:133], v[36:39], v[2:17]
	v_exp_f32_e32 v66, v66
	v_exp_f32_e32 v67, v67
	v_exp_f32_e32 v68, v68
	v_exp_f32_e32 v69, v69
	s_waitcnt lgkmcnt(12)
	v_mfma_f32_32x32x16_bf16 v[18:33], v[130:133], v[40:43], v[18:33]
	v_exp_f32_e32 v70, v70
	v_exp_f32_e32 v71, v71
	v_exp_f32_e32 v72, v72
	v_exp_f32_e32 v73, v73
	v_add_u32_e32 v36, s52, v232
	ds_read_b128 v[174:177], v36
	ds_read_b128 v[166:169], v36 offset:512
	s_waitcnt lgkmcnt(12)
	v_mfma_f32_32x32x16_bf16 v[2:17], v[134:137], v[44:47], v[2:17]
	v_exp_f32_e32 v74, v74
	v_exp_f32_e32 v75, v75
	v_exp_f32_e32 v76, v76
	v_exp_f32_e32 v77, v77
	ds_read_b128 v[170:173], v36 offset:2048
	ds_read_b128 v[158:161], v36 offset:2560
	s_waitcnt lgkmcnt(12)
	v_mfma_f32_32x32x16_bf16 v[18:33], v[134:137], v[98:101], v[18:33]
	v_exp_f32_e32 v78, v78
	v_exp_f32_e32 v79, v79
	v_exp_f32_e32 v80, v80
	v_exp_f32_e32 v81, v81
	ds_read_b128 v[162:165], v36 offset:4096
	ds_read_b128 v[150:153], v36 offset:4608
	s_waitcnt lgkmcnt(12)
	v_mfma_f32_32x32x16_bf16 v[2:17], v[138:141], v[102:105], v[2:17]
	v_exp_f32_e32 v50, v50
	v_exp_f32_e32 v51, v51
	v_exp_f32_e32 v52, v52
	v_exp_f32_e32 v53, v53
	ds_read_b128 v[154:157], v36 offset:6144
	ds_read_b128 v[146:149], v36 offset:6656
	s_waitcnt lgkmcnt(12)
	v_mfma_f32_32x32x16_bf16 v[18:33], v[138:141], v[82:85], v[18:33]
	v_exp_f32_e32 v54, v54
	v_exp_f32_e32 v55, v55
	v_exp_f32_e32 v56, v56
	v_exp_f32_e32 v57, v57
	s_waitcnt lgkmcnt(10)
	v_mfma_f32_32x32x16_bf16 v[2:17], v[142:145], v[86:89], v[2:17]
	v_exp_f32_e32 v58, v58
	v_exp_f32_e32 v59, v59
	v_exp_f32_e32 v60, v60
	v_exp_f32_e32 v61, v61
	s_waitcnt lgkmcnt(8)
	v_mfma_f32_32x32x16_bf16 v[18:33], v[142:145], v[90:93], v[18:33]
	v_exp_f32_e32 v62, v62
	v_exp_f32_e32 v63, v63
	v_exp_f32_e32 v64, v64
	v_exp_f32_e32 v65, v65
	s_waitcnt vmcnt(2) lgkmcnt(0)
	s_barrier
	s_add_i32 s41, s52, 0x2000
	s_cmpk_lg_i32 s52, 0x4000
	s_cselect_b32 s53, s41, 0
	v_lshl_add_u64 v[218:219], v[218:219], 0, s[14:15]
	v_lshl_add_u64 v[220:221], v[220:221], 0, s[14:15]
	v_add_u32_e32 v35, 0x200, v35
	s_cmp_ge_i32 s30, s9
	s_mov_b32 s42, s8
	s_cbranch_scc0 .LBB0_1702
	s_add_i32 s9, s30, 1
	s_cmp_ge_i32 s9, s49
	s_cbranch_scc1 .LBB0_1742
